# attention tile loop rotated: barrier moved in front of the last PV block (which reads registers only); the next tile's K/Q fragments are requested under it so the first score MFMAs start without an LD
# speedup vs baseline: 1.0040x; 1.0040x over previous
.LBB0_438:
	s_lshl_b32 s2, s12, 1
	s_and_b32 s2, s2, 14
	s_ashr_i32 s3, s12, 7
	s_add_i32 s2, s2, s3
	s_ashr_i32 s3, s2, 2
	s_lshl_b32 s22, s3, 8
	s_lshl_b32 s21, s3, 12
	s_lshl_b32 s3, s12, 5
	s_lshl_b32 s2, s2, 7
	v_mov_b32_e32 v205, v3
	v_readlane_b32 s8, v254, 27
	s_and_b32 s3, s3, 0xf00
	s_and_b32 s10, s2, 0x180
	v_mbcnt_lo_u32_b32 v0, -1, 0
	v_mbcnt_hi_u32_b32 v0, -1, v0
	s_add_i32 s13, s22, 0x4000
	v_add_u32_e32 v204, s8, v0
	s_or_b32 s11, s21, s3
	s_lshl_b32 s80, s10, 1
	s_add_u32 s2, s52, s80
	v_lshlrev_b32_e32 v0, 4, v204
	v_add_u32_e32 v6, 0x200, v204
	v_add_u32_e32 v12, 0x400, v204
	v_add_u32_e32 v14, 0x600, v204
	s_addc_u32 s3, s53, 0
	v_and_b32_e32 v2, 0xf0, v0
	v_ashrrev_i32_e32 v36, 4, v204
	v_ashrrev_i32_e32 v38, 4, v6
	v_ashrrev_i32_e32 v40, 4, v12
	v_ashrrev_i32_e32 v42, 4, v14
	v_add_u32_e32 v20, 0x800, v204
	v_add_u32_e32 v22, 0xa00, v204
	v_lshl_add_u64 v[0:1], s[2:3], 0, v[2:3]
	v_add_u32_e32 v4, s11, v36
	s_movk_i32 s18, 0x1400
	v_add_u32_e32 v6, s11, v38
	v_add_u32_e32 v12, s11, v40
	v_add_u32_e32 v14, s11, v42
	v_ashrrev_i32_e32 v44, 4, v20
	v_ashrrev_i32_e32 v46, 4, v22
	v_add_u32_e32 v28, 0xc00, v204
	v_add_u32_e32 v32, 0xe00, v204
	v_mad_i64_i32 v[4:5], s[8:9], v4, s18, v[0:1]
	v_mad_i64_i32 v[8:9], s[8:9], v6, s18, v[0:1]
	v_mad_i64_i32 v[12:13], s[8:9], v12, s18, v[0:1]
	v_mad_i64_i32 v[16:17], s[8:9], v14, s18, v[0:1]
	v_add_u32_e32 v20, s11, v44
	v_add_u32_e32 v22, s11, v46
	v_ashrrev_i32_e32 v47, 4, v28
	v_ashrrev_i32_e32 v48, 4, v32
	global_load_dwordx4 v[4:7], v[4:5], off
	s_nop 0
	global_load_dwordx4 v[8:11], v[8:9], off
	s_nop 0
	global_load_dwordx4 v[12:15], v[12:13], off
	s_nop 0
	global_load_dwordx4 v[16:19], v[16:17], off
	v_mad_i64_i32 v[20:21], s[8:9], v20, s18, v[0:1]
	v_mad_i64_i32 v[24:25], s[8:9], v22, s18, v[0:1]
	v_add_u32_e32 v28, s11, v47
	v_add_u32_e32 v32, s11, v48
	global_load_dwordx4 v[20:23], v[20:21], off
	s_nop 0
	global_load_dwordx4 v[24:27], v[24:25], off
	v_mad_i64_i32 v[28:29], s[8:9], v28, s18, v[0:1]
	v_mad_i64_i32 v[0:1], s[8:9], v32, s18, v[0:1]
	global_load_dwordx4 v[28:31], v[28:29], off
	v_add_u32_e32 v206, 0x11800, v205
	global_load_dwordx4 v[32:35], v[0:1], off
	v_add_u32_e32 v0, v206, v2
	v_mad_u64_u32 v[36:37], s[14:15], v36, s30, v[0:1]
	v_mad_u64_u32 v[38:39], s[14:15], v38, s30, v[0:1]
	v_mad_u64_u32 v[40:41], s[14:15], v40, s30, v[0:1]
	v_mad_u64_u32 v[42:43], s[14:15], v42, s30, v[0:1]
	v_mad_u64_u32 v[44:45], s[14:15], v44, s30, v[0:1]
	v_and_b32_e32 v2, 63, v204
	v_ashrrev_i32_e32 v49, 6, v204
	s_mov_b64 s[24:25], 0x400
	v_readfirstlane_b32 s8, v49
	s_mov_b32 s23, 0
	v_mov_b32_e32 v210, 0
	v_mov_b32_e32 v208, 0xf149f2ca
	v_mov_b32_e32 v209, 0xf149f2ca
	v_mov_b32_e32 v207, 0
	s_waitcnt vmcnt(7)
	ds_write_b128 v36, v[4:7]
	s_waitcnt vmcnt(6)
	ds_write_b128 v38, v[8:11]
	s_waitcnt vmcnt(5)
	ds_write_b128 v40, v[12:15]
	s_waitcnt vmcnt(4)
	ds_write_b128 v42, v[16:19]
	s_waitcnt vmcnt(3)
	ds_write_b128 v44, v[20:23]
	v_mad_u64_u32 v[4:5], s[14:15], v46, s30, v[0:1]
	s_waitcnt vmcnt(2)
	ds_write_b128 v4, v[24:27]
	v_mad_u64_u32 v[4:5], s[14:15], v47, s30, v[0:1]
	v_mad_u64_u32 v[0:1], s[14:15], v48, s30, v[0:1]
	s_waitcnt vmcnt(1)
	ds_write_b128 v4, v[28:31]
	s_waitcnt vmcnt(0)
	ds_write_b128 v0, v[32:35]
	v_or_b32_e32 v4, s13, v2
	v_mov_b64_e32 v[0:1], s[52:53]
	v_mad_i64_i32 v[0:1], s[14:15], v4, s18, v[0:1]
	s_lshl_b32 s14, s8, 3
	s_add_i32 s15, s21, 0xffffff00
	s_cmp_lt_i32 s8, 32
	s_cselect_b32 s9, s13, s15
	s_add_i32 s9, s9, s14
	s_mul_hi_i32 s18, s9, 0x1400
	s_mulk_i32 s9, 0x1400
	s_add_u32 s9, s52, s9
	v_lshlrev_b32_e32 v4, 3, v49
	s_addc_u32 s19, s53, s18
	v_lshl_add_u64 v[0:1], v[0:1], 0, s[80:81]
	v_ashrrev_i32_e32 v5, 31, v4
	s_add_u32 s18, s9, s80
	v_lshl_add_u64 v[0:1], v[4:5], 1, v[0:1]
	s_addc_u32 s19, s19, 0
	v_lshlrev_b32_e32 v2, 2, v2
	global_load_dwordx4 v[176:179], v[0:1], off offset:2048
	global_load_dwordx4 v[180:183], v[0:1], off offset:2176
	v_lshl_add_u64 v[0:1], s[18:19], 0, v[2:3]
	s_mul_i32 s19, s8, 0x880
	v_add_u32_e32 v4, s19, v205
	s_or_b32 s20, s14, 1
	v_readfirstlane_b32 s9, v4
	s_cmpk_lt_i32 s20, 0x100
	s_mov_b32 m0, s9
	s_cselect_b32 s9, s13, s15
	s_add_i32 s9, s9, s20
	s_mul_hi_i32 s18, s9, 0x1400
	s_mulk_i32 s9, 0x1400
	s_add_u32 s9, s52, s9
	s_mulk_i32 s20, 0x110
	s_addc_u32 s18, s53, s18
	v_add_u32_e32 v4, s20, v205
	v_lshl_add_u64 v[0:1], v[0:1], 0, s[24:25]
	s_add_u32 s26, s9, s80
	v_readfirstlane_b32 s9, v4
	global_load_lds_dword v[0:1], off
	s_addc_u32 s27, s18, 0
	s_mov_b32 m0, s9
	s_or_b32 s9, s14, 2
	s_cmpk_lt_i32 s9, 0x100
	s_cselect_b32 s18, s13, s15
	s_add_i32 s9, s18, s9
	s_mul_hi_i32 s18, s9, 0x1400
	s_mulk_i32 s9, 0x1400
	s_add_u32 s9, s52, s9
	s_addc_u32 s18, s53, s18
	v_lshl_add_u64 v[0:1], s[26:27], 0, v[2:3]
	s_add_u32 s26, s9, s80
	s_addc_u32 s27, s18, 0
	s_add_i32 s9, s20, 0x110
	v_add_u32_e32 v4, s9, v205
	v_lshl_add_u64 v[0:1], v[0:1], 0, s[24:25]
	v_readfirstlane_b32 s9, v4
	global_load_lds_dword v[0:1], off
	s_mov_b32 m0, s9
	s_or_b32 s9, s14, 3
	s_cmpk_lt_i32 s9, 0x100
	s_cselect_b32 s18, s13, s15
	s_add_i32 s9, s18, s9
	s_mul_hi_i32 s18, s9, 0x1400
	s_mulk_i32 s9, 0x1400
	s_add_u32 s9, s52, s9
	s_addc_u32 s18, s53, s18
	v_lshl_add_u64 v[0:1], s[26:27], 0, v[2:3]
	s_add_u32 s26, s9, s80
	s_addc_u32 s27, s18, 0
	s_add_i32 s9, s20, 0x220
	v_add_u32_e32 v4, s9, v205
	v_lshl_add_u64 v[0:1], v[0:1], 0, s[24:25]
	v_readfirstlane_b32 s9, v4
	global_load_lds_dword v[0:1], off
	s_mov_b32 m0, s9
	s_or_b32 s9, s14, 4
	s_cmpk_lt_i32 s9, 0x100
	s_cselect_b32 s18, s13, s15
	s_add_i32 s9, s18, s9
	s_mul_hi_i32 s18, s9, 0x1400
	s_mulk_i32 s9, 0x1400
	s_add_u32 s9, s52, s9
	s_addc_u32 s18, s53, s18
	v_lshl_add_u64 v[0:1], s[26:27], 0, v[2:3]
	s_add_u32 s26, s9, s80
	s_addc_u32 s27, s18, 0
	s_add_i32 s9, s20, 0x330
	v_add_u32_e32 v4, s9, v205
	v_lshl_add_u64 v[0:1], v[0:1], 0, s[24:25]
	v_readfirstlane_b32 s9, v4
	global_load_lds_dword v[0:1], off
	s_mov_b32 m0, s9
	s_or_b32 s9, s14, 5
	s_cmpk_lt_i32 s9, 0x100
	s_cselect_b32 s18, s13, s15
	s_add_i32 s9, s18, s9
	s_mul_hi_i32 s18, s9, 0x1400
	s_mulk_i32 s9, 0x1400
	s_add_u32 s9, s52, s9
	s_addc_u32 s18, s53, s18
	v_lshl_add_u64 v[0:1], s[26:27], 0, v[2:3]
	s_add_u32 s26, s9, s80
	s_addc_u32 s27, s18, 0
	s_add_i32 s9, s20, 0x440
	v_add_u32_e32 v4, s9, v205
	v_lshl_add_u64 v[0:1], v[0:1], 0, s[24:25]
	v_readfirstlane_b32 s9, v4
	global_load_lds_dword v[0:1], off
	s_mov_b32 m0, s9
	s_or_b32 s9, s14, 6
	s_cmpk_lt_i32 s9, 0x100
	s_cselect_b32 s18, s13, s15
	s_add_i32 s9, s18, s9
	s_mul_hi_i32 s18, s9, 0x1400
	s_mulk_i32 s9, 0x1400
	s_add_u32 s9, s52, s9
	s_addc_u32 s18, s53, s18
	v_lshl_add_u64 v[0:1], s[26:27], 0, v[2:3]
	s_add_u32 s26, s9, s80
	s_addc_u32 s27, s18, 0
	s_add_i32 s9, s20, 0x550
	v_add_u32_e32 v4, s9, v205
	v_lshl_add_u64 v[0:1], v[0:1], 0, s[24:25]
	v_readfirstlane_b32 s9, v4
	global_load_lds_dword v[0:1], off
	s_mov_b32 m0, s9
	s_or_b32 s9, s14, 7
	s_cmpk_lt_i32 s9, 0x100
	s_cselect_b32 s18, s13, s15
	s_add_i32 s9, s18, s9
	s_mul_hi_i32 s18, s9, 0x1400
	s_mulk_i32 s9, 0x1400
	s_add_u32 s9, s52, s9
	s_addc_u32 s18, s53, s18
	v_lshl_add_u64 v[0:1], s[26:27], 0, v[2:3]
	s_add_u32 s26, s9, s80
	v_lshl_add_u64 v[0:1], v[0:1], 0, s[24:25]
	s_addc_u32 s27, s18, 0
	s_add_i32 s9, s20, 0x660
	global_load_lds_dword v[0:1], off
	v_lshl_add_u64 v[0:1], s[26:27], 0, v[2:3]
	v_add_u32_e32 v2, s9, v205
	v_lshl_add_u64 v[0:1], v[0:1], 0, s[24:25]
	v_readfirstlane_b32 s9, v2
	s_mov_b32 m0, s9
	s_movk_i32 s9, 0x480
	global_load_lds_dword v[0:1], off
	v_bfe_u32 v0, v204, 2, 2
	v_and_b32_e32 v1, 12, v204
	v_cmp_ne_u32_e32 vcc, 2, v0
	v_mov_b32_e32 v14, v3
	v_mov_b32_e32 v15, v3
	v_cndmask_b32_e32 v1, 4, v1, vcc
	v_cmp_ne_u32_e32 vcc, 1, v0
	v_mov_b32_e32 v2, v3
	v_mov_b32_e32 v4, v3
	v_cndmask_b32_e32 v0, 8, v1, vcc
	v_and_or_b32 v0, v204, 51, v0
	v_mul_lo_u32 v1, v49, s9
	v_lshlrev_b32_e32 v0, 1, v0
	v_add3_u32 v0, v205, v1, v0
	s_waitcnt vmcnt(0)
	ds_write_b16 v0, v176 offset:34816
	ds_write_b16_d16_hi v0, v176 offset:34960
	ds_write_b16 v0, v177 offset:35104
	ds_write_b16_d16_hi v0, v177 offset:35248
	ds_write_b16 v0, v178 offset:35392
	ds_write_b16_d16_hi v0, v178 offset:35536
	ds_write_b16 v0, v179 offset:35680
	ds_write_b16_d16_hi v0, v179 offset:35824
	ds_write_b16 v0, v180 offset:44032
	ds_write_b16_d16_hi v0, v180 offset:44176
	ds_write_b16 v0, v181 offset:44320
	ds_write_b16_d16_hi v0, v181 offset:44464
	ds_write_b16 v0, v182 offset:44608
	ds_write_b16_d16_hi v0, v182 offset:44752
	ds_write_b16 v0, v183 offset:44896
	ds_write_b16_d16_hi v0, v183 offset:45040
	v_mov_b32_e32 v0, v3
	v_mov_b32_e32 v1, v3
	v_mov_b32_e32 v5, v3
	v_mov_b32_e32 v6, v3
	v_mov_b32_e32 v7, v3
	v_mov_b32_e32 v8, v3
	v_mov_b32_e32 v9, v3
	v_mov_b32_e32 v10, v3
	v_mov_b32_e32 v11, v3
	v_mov_b32_e32 v12, v3
	v_mov_b32_e32 v13, v3
	v_mov_b64_e32 v[30:31], v[14:15]
	v_mov_b64_e32 v[62:63], v[14:15]
	v_mov_b64_e32 v[94:95], v[14:15]
	v_mov_b64_e32 v[126:127], v[14:15]
	v_mov_b64_e32 v[46:47], v[14:15]
	v_mov_b64_e32 v[78:79], v[14:15]
	v_mov_b64_e32 v[110:111], v[14:15]
	v_mov_b64_e32 v[142:143], v[14:15]
	s_lshl_b32 s18, s8, 5
	s_addk_i32 s21, 0xff40
	s_addk_i32 s22, 0x4040
	v_mov_b64_e32 v[28:29], v[12:13]
	v_mov_b64_e32 v[26:27], v[10:11]
	v_mov_b64_e32 v[24:25], v[8:9]
	v_mov_b64_e32 v[22:23], v[6:7]
	v_mov_b64_e32 v[20:21], v[4:5]
	v_mov_b64_e32 v[18:19], v[2:3]
	v_mov_b64_e32 v[16:17], v[0:1]
	v_mov_b64_e32 v[60:61], v[12:13]
	v_mov_b64_e32 v[58:59], v[10:11]
	v_mov_b64_e32 v[56:57], v[8:9]
	v_mov_b64_e32 v[54:55], v[6:7]
	v_mov_b64_e32 v[52:53], v[4:5]
	v_mov_b64_e32 v[50:51], v[2:3]
	v_mov_b64_e32 v[48:49], v[0:1]
	v_mov_b64_e32 v[92:93], v[12:13]
	v_mov_b64_e32 v[90:91], v[10:11]
	v_mov_b64_e32 v[88:89], v[8:9]
	v_mov_b64_e32 v[86:87], v[6:7]
	v_mov_b64_e32 v[84:85], v[4:5]
	v_mov_b64_e32 v[82:83], v[2:3]
	v_mov_b64_e32 v[80:81], v[0:1]
	v_mov_b64_e32 v[124:125], v[12:13]
	v_mov_b64_e32 v[122:123], v[10:11]
	v_mov_b64_e32 v[120:121], v[8:9]
	v_mov_b64_e32 v[118:119], v[6:7]
	v_mov_b64_e32 v[116:117], v[4:5]
	v_mov_b64_e32 v[114:115], v[2:3]
	v_mov_b64_e32 v[112:113], v[0:1]
	v_mov_b64_e32 v[44:45], v[12:13]
	v_mov_b64_e32 v[42:43], v[10:11]
	v_mov_b64_e32 v[40:41], v[8:9]
	v_mov_b64_e32 v[38:39], v[6:7]
	v_mov_b64_e32 v[36:37], v[4:5]
	v_mov_b64_e32 v[34:35], v[2:3]
	v_mov_b64_e32 v[32:33], v[0:1]
	v_mov_b64_e32 v[76:77], v[12:13]
	v_mov_b64_e32 v[74:75], v[10:11]
	v_mov_b64_e32 v[72:73], v[8:9]
	v_mov_b64_e32 v[70:71], v[6:7]
	v_mov_b64_e32 v[68:69], v[4:5]
	v_mov_b64_e32 v[66:67], v[2:3]
	v_mov_b64_e32 v[64:65], v[0:1]
	v_mov_b64_e32 v[108:109], v[12:13]
	v_mov_b64_e32 v[106:107], v[10:11]
	v_mov_b64_e32 v[104:105], v[8:9]
	v_mov_b64_e32 v[102:103], v[6:7]
	v_mov_b64_e32 v[100:101], v[4:5]
	v_mov_b64_e32 v[98:99], v[2:3]
	v_mov_b64_e32 v[96:97], v[0:1]
	v_mov_b64_e32 v[140:141], v[12:13]
	v_mov_b64_e32 v[138:139], v[10:11]
	v_mov_b64_e32 v[136:137], v[8:9]
	v_mov_b64_e32 v[134:135], v[6:7]
	v_mov_b64_e32 v[132:133], v[4:5]
	v_mov_b64_e32 v[130:131], v[2:3]
	v_mov_b64_e32 v[128:129], v[0:1]
	s_mov_b32 s26, 0
	s_waitcnt lgkmcnt(0)
	s_barrier
	v_and_b32_e32 v2, 31, v204
	v_bfe_u32 v15, v204, 5, 1
	v_lshlrev_b32_e32 v15, 4, v15
	v_or_b32_e32 v13, s18, v2
	v_mul_u32_u24_e32 v1, 0x90, v2
	v_mad_u32_u24 v0, v2, s30, v15
	v_mul_lo_u32 v13, v13, s30
	v_add_u32_e32 v0, v0, v205
	v_add3_u32 v1, v1, v15, v205
	v_add3_u32 v13, v206, v13, v15
	v_bfe_u32 v15, v204, 2, 2
	v_and_b32_e32 v2, 12, v204
	v_cmp_ne_u32_e32 vcc, 2, v15
	s_movk_i32 s8, 0x480
	v_ashrrev_i32_e32 v211, 6, v204
	v_cndmask_b32_e32 v2, 4, v2, vcc
	v_cmp_ne_u32_e32 vcc, 1, v15
	v_mul_lo_u32 v211, v211, s8
	s_nop 0
	v_cndmask_b32_e32 v15, 8, v2, vcc
	v_and_or_b32 v2, v204, 51, v15
	v_lshlrev_b32_e32 v2, 1, v2
	v_add3_u32 v2, v205, v211, v2
	v_and_b32_e32 v206, 63, v204
	v_ashrrev_i32_e32 v252, 6, v204
	s_movk_i32 s8, 0x1400
	v_lshlrev_b32_e32 v252, 4, v252
	v_mad_u32_u24 v252, v206, s8, v252
	v_lshlrev_b32_e32 v206, 2, v206
	v_add_u32_e32 v206, 0x400, v206
	v_mov_b32_e32 v12, v0
	ds_read_b128 v[228:231], v12 offset:0
	ds_read_b128 v[232:235], v12 offset:32
	ds_read_b128 v[236:239], v12 offset:64
	ds_read_b128 v[240:243], v12 offset:96
	ds_read_b128 v[244:247], v13 offset:0
	ds_read_b128 v[248:251], v13 offset:32
	ds_read_b128 v[4:7], v13 offset:64
	ds_read_b128 v[8:11], v13 offset:96
.LBB0_439:
	s_add_i32 s25, s26, 1
	s_and_b32 s27, s26, 1
	s_mul_i32 s24, s27, 0x4400
	s_mul_i32 s31, s27, 0x4800
	v_add_u32_e32 v12, s24, v0
	v_add_u32_e32 v14, s31, v1
	ds_read_b128 v[184:187], v14 offset:34816
	ds_read_b128 v[188:191], v14 offset:39424
	ds_read_b128 v[192:195], v14 offset:44032
	ds_read_b128 v[196:199], v14 offset:48640
	ds_read_b128 v[200:203], v14 offset:34848
	ds_read_b128 v[212:215], v14 offset:39456
	ds_read_b128 v[216:219], v14 offset:44064
	s_cmpk_gt_u32 s26, 0x42
	s_waitcnt lgkmcnt(7)
	ds_read_b128 v[220:223], v14 offset:48672
	s_cbranch_scc1 .Lat_noload
	v_mfma_f32_32x32x16_bf16 v[144:159], v[228:231], v[244:247], 0
	s_cmp_lt_u32 s26, 3
	s_cselect_b32 s24, s22, s21
	s_cselect_b32 s31, s13, s15
	s_add_i32 s24, s24, s23
	s_add_i32 s31, s31, s14
	s_mul_hi_i32 s37, s24, 0x1400
	s_mul_i32 s36, s24, 0x1400
	s_add_i32 s31, s31, s23
	s_add_u32 s36, s2, s36
	s_addc_u32 s37, s3, s37
	s_add_i32 s31, s31, 64
	global_load_dwordx4 v[176:179], v252, s[36:37] offset:2048
	global_load_dwordx4 v[180:183], v252, s[36:37] offset:2176
	s_mul_hi_i32 s37, s31, 0x1400
	s_mul_i32 s36, s31, 0x1400
	s_add_u32 s36, s2, s36
	v_mfma_f32_32x32x16_bf16 v[144:159], v[232:235], v[248:251], v[144:159]
	s_addc_u32 s37, s3, s37
	v_readfirstlane_b32 s38, v205
	s_xor_b32 s39, s27, 1
	s_mul_i32 s39, s39, 0x4400
	s_add_i32 s38, s38, s19
	s_add_i32 s38, s38, s39
	s_add_i32 m0, s38, 0
	s_nop 0
	global_load_lds_dword v206, s[36:37]
	s_add_u32 s36, s36, 0x1400
	s_addc_u32 s37, s37, 0
	s_add_i32 m0, s38, 272
	s_nop 0
	global_load_lds_dword v206, s[36:37]
	s_add_u32 s36, s36, 0x1400
	v_mfma_f32_32x32x16_bf16 v[144:159], v[236:239], v[4:7], v[144:159]
	s_addc_u32 s37, s37, 0
	s_add_i32 m0, s38, 544
	s_nop 0
	global_load_lds_dword v206, s[36:37]
	s_add_u32 s36, s36, 0x1400
	s_addc_u32 s37, s37, 0
	s_add_i32 m0, s38, 816
	s_nop 0
	global_load_lds_dword v206, s[36:37]
	s_add_u32 s36, s36, 0x1400
	s_addc_u32 s37, s37, 0
	s_add_i32 m0, s38, 1088
	s_nop 0
	global_load_lds_dword v206, s[36:37]
	s_add_u32 s36, s36, 0x1400
	v_mfma_f32_32x32x16_bf16 v[144:159], v[240:243], v[8:11], v[144:159]
	s_addc_u32 s37, s37, 0
	s_add_i32 m0, s38, 1360
	s_nop 0
	global_load_lds_dword v206, s[36:37]
	s_add_u32 s36, s36, 0x1400
	s_addc_u32 s37, s37, 0
	s_add_i32 m0, s38, 1632
	s_nop 0
	global_load_lds_dword v206, s[36:37]
	s_add_u32 s36, s36, 0x1400
	s_addc_u32 s37, s37, 0
	s_add_i32 m0, s38, 1904
	s_nop 0
	global_load_lds_dword v206, s[36:37]
	s_branch .Lat_join

.Lat_back1_s1:
	v_sub_f32_e32 v160, v160, v208
	v_sub_f32_e32 v161, v161, v208
	v_sub_f32_e32 v162, v162, v208
	v_sub_f32_e32 v163, v163, v208
	v_mfma_f32_32x32x16_bf16 v[96:111], v[188:191], v[144:147], v[96:111]
	v_exp_f32_e32 v160, v160
	v_exp_f32_e32 v161, v161
	v_exp_f32_e32 v162, v162
	v_exp_f32_e32 v163, v163
	v_sub_f32_e32 v164, v164, v208
	v_sub_f32_e32 v165, v165, v208
	v_sub_f32_e32 v166, v166, v208
	v_sub_f32_e32 v167, v167, v208
	v_mfma_f32_32x32x16_bf16 v[64:79], v[192:195], v[144:147], v[64:79]
	v_exp_f32_e32 v164, v164
	v_exp_f32_e32 v165, v165
	v_exp_f32_e32 v166, v166
	v_exp_f32_e32 v167, v167
	v_sub_f32_e32 v168, v168, v208
	v_sub_f32_e32 v169, v169, v208
	v_sub_f32_e32 v170, v170, v208
	v_sub_f32_e32 v171, v171, v208
	v_mfma_f32_32x32x16_bf16 v[32:47], v[196:199], v[144:147], v[32:47]
	v_exp_f32_e32 v168, v168
	v_exp_f32_e32 v169, v169
	v_exp_f32_e32 v170, v170
	v_exp_f32_e32 v171, v171
	v_sub_f32_e32 v172, v172, v208
	v_sub_f32_e32 v173, v173, v208
	v_sub_f32_e32 v174, v174, v208
	v_sub_f32_e32 v175, v175, v208
	v_mfma_f32_32x32x16_bf16 v[128:143], v[200:203], v[148:151], v[128:143]
	v_exp_f32_e32 v172, v172
	v_exp_f32_e32 v173, v173
	v_exp_f32_e32 v174, v174
	v_exp_f32_e32 v175, v175
	v_add_f32_e32 v15, v160, v161
	v_add_f32_e32 v211, v162, v163
	v_add_f32_e32 v15, v15, v211
	v_add_f32_e32 v211, v164, v165
	v_mfma_f32_32x32x16_bf16 v[96:111], v[212:215], v[148:151], v[96:111]
	v_add_f32_e32 v224, v166, v167
	v_add_f32_e32 v211, v211, v224
	v_add_f32_e32 v224, v168, v169
	v_add_f32_e32 v225, v170, v171
	v_add_f32_e32 v224, v224, v225
	v_add_f32_e32 v225, v172, v173
	v_add_f32_e32 v227, v174, v175
	v_add_f32_e32 v225, v225, v227
	v_add_f32_e32 v15, v15, v211
	v_add_f32_e32 v224, v224, v225
	v_add_f32_e32 v15, v15, v224
	v_add_f32_e32 v207, v207, v15
	v_cvt_pk_bf16_f32 v160, v160, v161
	v_cvt_pk_bf16_f32 v161, v162, v163
	v_cvt_pk_bf16_f32 v162, v164, v165
	v_cvt_pk_bf16_f32 v163, v166, v167
	v_cvt_pk_bf16_f32 v164, v168, v169
	v_cvt_pk_bf16_f32 v165, v170, v171
	v_cvt_pk_bf16_f32 v166, v172, v173
	v_cvt_pk_bf16_f32 v167, v174, v175
	v_mfma_f32_32x32x16_bf16 v[64:79], v[216:219], v[148:151], v[64:79]
	s_xor_b32 s8, s27, 1
	s_mulk_i32 s8, 0x4800
	s_waitcnt vmcnt(0)
	v_add_u32_e32 v15, s8, v2
	ds_write_b16 v15, v176 offset:34816
	ds_write_b16_d16_hi v15, v176 offset:34960
	ds_write_b16 v15, v177 offset:35104
	ds_write_b16_d16_hi v15, v177 offset:35248
	ds_write_b16 v15, v178 offset:35392
	ds_write_b16_d16_hi v15, v178 offset:35536
	ds_write_b16 v15, v179 offset:35680
	ds_write_b16_d16_hi v15, v179 offset:35824
	ds_write_b16 v15, v180 offset:44032
	ds_write_b16_d16_hi v15, v180 offset:44176
	ds_write_b16 v15, v181 offset:44320
	ds_write_b16_d16_hi v15, v181 offset:44464
	ds_write_b16 v15, v182 offset:44608
	ds_write_b16_d16_hi v15, v182 offset:44752
	ds_write_b16 v15, v183 offset:44896
	ds_write_b16_d16_hi v15, v183 offset:45040
	v_mfma_f32_32x32x16_bf16 v[32:47], v[220:223], v[148:151], v[32:47]
	s_add_i32 s23, s23, 64
	s_cmpk_lg_i32 s23, 0x1100
	s_waitcnt vmcnt(0) lgkmcnt(0)
	s_barrier
	s_cbranch_scc0 .Lat_last
	s_and_b32 s8, s25, 1
	s_mul_i32 s8, s8, 0x4400
	v_add_u32_e32 v12, s8, v0
	v_mfma_f32_32x32x16_bf16 v[112:127], v[184:187], v[160:163], v[112:127]
	ds_read_b128 v[228:231], v12 offset:0
	v_mfma_f32_32x32x16_bf16 v[80:95], v[188:191], v[160:163], v[80:95]
	ds_read_b128 v[232:235], v12 offset:32
	v_mfma_f32_32x32x16_bf16 v[48:63], v[192:195], v[160:163], v[48:63]
	ds_read_b128 v[236:239], v12 offset:64
	v_mfma_f32_32x32x16_bf16 v[16:31], v[196:199], v[160:163], v[16:31]
	ds_read_b128 v[240:243], v12 offset:96
	v_mfma_f32_32x32x16_bf16 v[112:127], v[200:203], v[164:167], v[112:127]
	ds_read_b128 v[244:247], v13 offset:0
	v_mfma_f32_32x32x16_bf16 v[80:95], v[212:215], v[164:167], v[80:95]
	ds_read_b128 v[248:251], v13 offset:32
	v_mfma_f32_32x32x16_bf16 v[48:63], v[216:219], v[164:167], v[48:63]
	ds_read_b128 v[4:7], v13 offset:64
	v_mfma_f32_32x32x16_bf16 v[16:31], v[220:223], v[164:167], v[16:31]
	ds_read_b128 v[8:11], v13 offset:96
	s_mov_b32 s26, s25
	s_branch .LBB0_439
.Lat_last:
	v_mfma_f32_32x32x16_bf16 v[112:127], v[184:187], v[160:163], v[112:127]
	v_mfma_f32_32x32x16_bf16 v[80:95], v[188:191], v[160:163], v[80:95]
	v_mfma_f32_32x32x16_bf16 v[48:63], v[192:195], v[160:163], v[48:63]
	v_mfma_f32_32x32x16_bf16 v[16:31], v[196:199], v[160:163], v[16:31]
	v_mfma_f32_32x32x16_bf16 v[112:127], v[200:203], v[164:167], v[112:127]
	v_mfma_f32_32x32x16_bf16 v[80:95], v[212:215], v[164:167], v[80:95]
	v_mfma_f32_32x32x16_bf16 v[48:63], v[216:219], v[164:167], v[48:63]
	v_mfma_f32_32x32x16_bf16 v[16:31], v[220:223], v[164:167], v[16:31]

.LBB0_745:
	s_and_b64 vcc, exec, s[0:1]
	s_cbranch_vccz .LBB0_454
	s_ashr_i32 s0, s22, 2
	s_lshl_b32 s15, s0, 8
	s_lshl_b32 s12, s0, 12
	s_lshl_b32 s0, s22, 7
	v_mov_b32_e32 v205, v3
	v_readlane_b32 s1, v254, 27
	s_and_b32 s8, s0, 0x180
	v_mbcnt_lo_u32_b32 v0, -1, 0
	v_mbcnt_hi_u32_b32 v0, -1, v0
	s_add_i32 s9, s15, 0x4000
	v_add_u32_e32 v204, s1, v0
	s_lshl_b32 s80, s8, 1
	s_add_u32 s0, s52, s80
	v_lshlrev_b32_e32 v0, 4, v204
	v_add_u32_e32 v6, 0x200, v204
	v_add_u32_e32 v12, 0x400, v204
	v_add_u32_e32 v14, 0x600, v204
	v_add_u32_e32 v20, 0x800, v204
	v_add_u32_e32 v22, 0xa00, v204
	v_add_u32_e32 v28, 0xc00, v204
	v_add_u32_e32 v32, 0xe00, v204
	s_addc_u32 s1, s53, 0
	v_and_b32_e32 v2, 0xf0, v0
	v_ashrrev_i32_e32 v36, 4, v204
	v_ashrrev_i32_e32 v38, 4, v6
	v_ashrrev_i32_e32 v40, 4, v12
	v_ashrrev_i32_e32 v42, 4, v14
	v_ashrrev_i32_e32 v44, 4, v20
	v_ashrrev_i32_e32 v46, 4, v22
	v_ashrrev_i32_e32 v48, 4, v28
	v_ashrrev_i32_e32 v50, 4, v32
	v_lshl_add_u64 v[0:1], s[0:1], 0, v[2:3]
	v_add_u32_e32 v4, s9, v36
	s_movk_i32 s13, 0x1400
	v_add_u32_e32 v6, s9, v38
	v_add_u32_e32 v12, s9, v40
	v_add_u32_e32 v14, s9, v42
	v_add_u32_e32 v20, s9, v44
	v_add_u32_e32 v22, s9, v46
	v_add_u32_e32 v28, s9, v48
	v_add_u32_e32 v32, s9, v50
	v_mad_i64_i32 v[4:5], s[2:3], v4, s13, v[0:1]
	v_mad_i64_i32 v[8:9], s[2:3], v6, s13, v[0:1]
	v_mad_i64_i32 v[12:13], s[2:3], v12, s13, v[0:1]
	v_mad_i64_i32 v[16:17], s[2:3], v14, s13, v[0:1]
	v_mad_i64_i32 v[20:21], s[2:3], v20, s13, v[0:1]
	v_mad_i64_i32 v[24:25], s[2:3], v22, s13, v[0:1]
	v_mad_i64_i32 v[28:29], s[2:3], v28, s13, v[0:1]
	v_mad_i64_i32 v[0:1], s[2:3], v32, s13, v[0:1]
	global_load_dwordx4 v[4:7], v[4:5], off
	s_nop 0
	global_load_dwordx4 v[8:11], v[8:9], off
	s_nop 0
	global_load_dwordx4 v[12:15], v[12:13], off
	s_nop 0
	global_load_dwordx4 v[16:19], v[16:17], off
	s_nop 0
	global_load_dwordx4 v[20:23], v[20:21], off
	s_nop 0
	global_load_dwordx4 v[24:27], v[24:25], off
	v_add_u32_e32 v206, 0x11800, v205
	global_load_dwordx4 v[28:31], v[28:29], off
	v_ashrrev_i32_e32 v51, 6, v204
	global_load_dwordx4 v[32:35], v[0:1], off
	v_add_u32_e32 v0, v206, v2
	v_mad_u64_u32 v[36:37], s[10:11], v36, s30, v[0:1]
	v_mad_u64_u32 v[38:39], s[10:11], v38, s30, v[0:1]
	v_mad_u64_u32 v[40:41], s[10:11], v40, s30, v[0:1]
	v_mad_u64_u32 v[42:43], s[10:11], v42, s30, v[0:1]
	v_mad_u64_u32 v[44:45], s[10:11], v44, s30, v[0:1]
	v_mad_u64_u32 v[46:47], s[10:11], v46, s30, v[0:1]
	v_mad_u64_u32 v[48:49], s[10:11], v48, s30, v[0:1]
	v_mad_u64_u32 v[0:1], s[10:11], v50, s30, v[0:1]
	v_and_b32_e32 v2, 63, v204
	v_readfirstlane_b32 s2, v51
	s_mov_b64 s[24:25], 0x400
	v_mov_b32_e32 v226, 0x3ecc95a3
	v_mov_b32_e32 v210, 0
	v_mov_b32_e32 v208, 0xf149f2ca
	s_waitcnt vmcnt(7)
	ds_write_b128 v36, v[4:7]
	s_waitcnt vmcnt(6)
	ds_write_b128 v38, v[8:11]
	s_waitcnt vmcnt(5)
	ds_write_b128 v40, v[12:15]
	s_waitcnt vmcnt(4)
	ds_write_b128 v42, v[16:19]
	s_waitcnt vmcnt(3)
	ds_write_b128 v44, v[20:23]
	s_waitcnt vmcnt(2)
	ds_write_b128 v46, v[24:27]
	s_waitcnt vmcnt(1)
	ds_write_b128 v48, v[28:31]
	v_or_b32_e32 v4, s9, v2
	v_lshlrev_b32_e32 v2, 2, v2
	v_mov_b32_e32 v14, v3
	s_waitcnt vmcnt(0)
	ds_write_b128 v0, v[32:35]
	v_mov_b64_e32 v[0:1], s[52:53]
	v_mad_i64_i32 v[0:1], s[10:11], v4, s13, v[0:1]
	s_lshl_b32 s10, s2, 3
	s_add_i32 s11, s12, 0xffffff00
	s_cmp_lt_i32 s2, 32
	s_cselect_b32 s3, s9, s11
	s_add_i32 s3, s3, s10
	s_mul_hi_i32 s12, s3, 0x1400
	s_mulk_i32 s3, 0x1400
	s_add_u32 s3, s52, s3
	v_lshlrev_b32_e32 v4, 3, v51
	s_addc_u32 s13, s53, s12
	v_lshl_add_u64 v[0:1], v[0:1], 0, s[80:81]
	v_ashrrev_i32_e32 v5, 31, v4
	s_add_u32 s12, s3, s80
	v_lshl_add_u64 v[0:1], v[4:5], 1, v[0:1]
	s_addc_u32 s13, s13, 0
	global_load_dwordx4 v[176:179], v[0:1], off offset:2048
	global_load_dwordx4 v[180:183], v[0:1], off offset:2176
	v_lshl_add_u64 v[0:1], s[12:13], 0, v[2:3]
	s_mul_i32 s13, s2, 0x880
	v_add_u32_e32 v4, s13, v205
	s_or_b32 s14, s10, 1
	v_readfirstlane_b32 s3, v4
	s_cmpk_lt_i32 s14, 0x100
	s_mov_b32 m0, s3
	s_cselect_b32 s3, s9, s11
	s_add_i32 s3, s3, s14
	s_mul_hi_i32 s12, s3, 0x1400
	s_mulk_i32 s3, 0x1400
	s_add_u32 s3, s52, s3
	s_mulk_i32 s14, 0x110
	s_addc_u32 s12, s53, s12
	v_add_u32_e32 v4, s14, v205
	v_lshl_add_u64 v[0:1], v[0:1], 0, s[24:25]
	s_add_u32 s22, s3, s80
	v_readfirstlane_b32 s3, v4
	global_load_lds_dword v[0:1], off
	s_addc_u32 s23, s12, 0
	s_mov_b32 m0, s3
	s_or_b32 s3, s10, 2
	s_cmpk_lt_i32 s3, 0x100
	s_cselect_b32 s12, s9, s11
	s_add_i32 s3, s12, s3
	s_mul_hi_i32 s12, s3, 0x1400
	s_mulk_i32 s3, 0x1400
	s_add_u32 s3, s52, s3
	s_addc_u32 s12, s53, s12
	v_lshl_add_u64 v[0:1], s[22:23], 0, v[2:3]
	s_add_u32 s22, s3, s80
	s_addc_u32 s23, s12, 0
	s_add_i32 s3, s14, 0x110
	v_add_u32_e32 v4, s3, v205
	v_lshl_add_u64 v[0:1], v[0:1], 0, s[24:25]
	v_readfirstlane_b32 s3, v4
	global_load_lds_dword v[0:1], off
	s_mov_b32 m0, s3
	s_or_b32 s3, s10, 3
	s_cmpk_lt_i32 s3, 0x100
	s_cselect_b32 s12, s9, s11
	s_add_i32 s3, s12, s3
	s_mul_hi_i32 s12, s3, 0x1400
	s_mulk_i32 s3, 0x1400
	s_add_u32 s3, s52, s3
	s_addc_u32 s12, s53, s12
	v_lshl_add_u64 v[0:1], s[22:23], 0, v[2:3]
	s_add_u32 s22, s3, s80
	s_addc_u32 s23, s12, 0
	s_add_i32 s3, s14, 0x220
	v_add_u32_e32 v4, s3, v205
	v_lshl_add_u64 v[0:1], v[0:1], 0, s[24:25]
	v_readfirstlane_b32 s3, v4
	global_load_lds_dword v[0:1], off
	s_mov_b32 m0, s3
	s_or_b32 s3, s10, 4
	s_cmpk_lt_i32 s3, 0x100
	s_cselect_b32 s12, s9, s11
	s_add_i32 s3, s12, s3
	s_mul_hi_i32 s12, s3, 0x1400
	s_mulk_i32 s3, 0x1400
	s_add_u32 s3, s52, s3
	s_addc_u32 s12, s53, s12
	v_lshl_add_u64 v[0:1], s[22:23], 0, v[2:3]
	s_add_u32 s22, s3, s80
	s_addc_u32 s23, s12, 0
	s_add_i32 s3, s14, 0x330
	v_add_u32_e32 v4, s3, v205
	v_lshl_add_u64 v[0:1], v[0:1], 0, s[24:25]
	v_readfirstlane_b32 s3, v4
	global_load_lds_dword v[0:1], off
	s_mov_b32 m0, s3
	s_or_b32 s3, s10, 5
	s_cmpk_lt_i32 s3, 0x100
	s_cselect_b32 s12, s9, s11
	s_add_i32 s3, s12, s3
	s_mul_hi_i32 s12, s3, 0x1400
	s_mulk_i32 s3, 0x1400
	s_add_u32 s3, s52, s3
	s_addc_u32 s12, s53, s12
	v_lshl_add_u64 v[0:1], s[22:23], 0, v[2:3]
	s_add_u32 s22, s3, s80
	s_addc_u32 s23, s12, 0
	s_add_i32 s3, s14, 0x440
	v_add_u32_e32 v4, s3, v205
	v_lshl_add_u64 v[0:1], v[0:1], 0, s[24:25]
	v_readfirstlane_b32 s3, v4
	global_load_lds_dword v[0:1], off
	s_mov_b32 m0, s3
	s_or_b32 s3, s10, 6
	s_cmpk_lt_i32 s3, 0x100
	s_cselect_b32 s12, s9, s11
	s_add_i32 s3, s12, s3
	s_mul_hi_i32 s12, s3, 0x1400
	s_mulk_i32 s3, 0x1400
	s_add_u32 s3, s52, s3
	s_addc_u32 s12, s53, s12
	v_lshl_add_u64 v[0:1], s[22:23], 0, v[2:3]
	s_add_u32 s22, s3, s80
	s_addc_u32 s23, s12, 0
	s_add_i32 s3, s14, 0x550
	v_add_u32_e32 v4, s3, v205
	v_lshl_add_u64 v[0:1], v[0:1], 0, s[24:25]
	v_readfirstlane_b32 s3, v4
	global_load_lds_dword v[0:1], off
	s_mov_b32 m0, s3
	s_or_b32 s3, s10, 7
	s_cmpk_lt_i32 s3, 0x100
	s_cselect_b32 s12, s9, s11
	s_add_i32 s3, s12, s3
	s_mul_hi_i32 s12, s3, 0x1400
	s_mulk_i32 s3, 0x1400
	s_add_u32 s3, s52, s3
	s_addc_u32 s12, s53, s12
	v_lshl_add_u64 v[0:1], s[22:23], 0, v[2:3]
	s_add_u32 s22, s3, s80
	v_lshl_add_u64 v[0:1], v[0:1], 0, s[24:25]
	s_addc_u32 s23, s12, 0
	s_add_i32 s3, s14, 0x660
	global_load_lds_dword v[0:1], off
	v_lshl_add_u64 v[0:1], s[22:23], 0, v[2:3]
	v_add_u32_e32 v2, s3, v205
	v_lshl_add_u64 v[0:1], v[0:1], 0, s[24:25]
	v_readfirstlane_b32 s3, v2
	s_mov_b32 m0, s3
	s_movk_i32 s3, 0x480
	global_load_lds_dword v[0:1], off
	v_bfe_u32 v0, v204, 2, 2
	v_and_b32_e32 v1, 12, v204
	v_cmp_ne_u32_e32 vcc, 2, v0
	v_mov_b32_e32 v15, v3
	v_mov_b32_e32 v2, v3
	v_cndmask_b32_e32 v1, 4, v1, vcc
	v_cmp_ne_u32_e32 vcc, 1, v0
	v_mov_b32_e32 v4, v3
	v_mov_b32_e32 v5, v3
	v_cndmask_b32_e32 v0, 8, v1, vcc
	v_and_or_b32 v0, v204, 51, v0
	v_mul_lo_u32 v1, v51, s3
	v_lshlrev_b32_e32 v0, 1, v0
	v_add3_u32 v0, v205, v1, v0
	s_waitcnt vmcnt(0)
	ds_write_b16 v0, v176 offset:34816
	ds_write_b16_d16_hi v0, v176 offset:34960
	ds_write_b16 v0, v177 offset:35104
	ds_write_b16_d16_hi v0, v177 offset:35248
	ds_write_b16 v0, v178 offset:35392
	ds_write_b16_d16_hi v0, v178 offset:35536
	ds_write_b16 v0, v179 offset:35680
	ds_write_b16_d16_hi v0, v179 offset:35824
	ds_write_b16 v0, v180 offset:44032
	ds_write_b16_d16_hi v0, v180 offset:44176
	ds_write_b16 v0, v181 offset:44320
	ds_write_b16_d16_hi v0, v181 offset:44464
	ds_write_b16 v0, v182 offset:44608
	ds_write_b16_d16_hi v0, v182 offset:44752
	ds_write_b16 v0, v183 offset:44896
	ds_write_b16_d16_hi v0, v183 offset:45040
	v_mov_b32_e32 v0, v3
	v_mov_b32_e32 v1, v3
	v_mov_b32_e32 v6, v3
	v_mov_b32_e32 v7, v3
	v_mov_b32_e32 v8, v3
	v_mov_b32_e32 v9, v3
	v_mov_b32_e32 v10, v3
	v_mov_b32_e32 v11, v3
	v_mov_b32_e32 v12, v3
	v_mov_b32_e32 v13, v3
	v_mov_b64_e32 v[30:31], v[14:15]
	v_mov_b64_e32 v[62:63], v[14:15]
	v_mov_b64_e32 v[94:95], v[14:15]
	v_mov_b64_e32 v[126:127], v[14:15]
	v_mov_b64_e32 v[46:47], v[14:15]
	v_mov_b64_e32 v[78:79], v[14:15]
	v_mov_b64_e32 v[110:111], v[14:15]
	v_mov_b64_e32 v[142:143], v[14:15]
	s_lshl_b32 s12, s2, 5
	s_addk_i32 s15, 0x4040
	s_mov_b32 s22, 0
	v_mov_b64_e32 v[28:29], v[12:13]
	v_mov_b64_e32 v[26:27], v[10:11]
	v_mov_b64_e32 v[24:25], v[8:9]
	v_mov_b64_e32 v[22:23], v[6:7]
	v_mov_b64_e32 v[20:21], v[4:5]
	v_mov_b64_e32 v[18:19], v[2:3]
	v_mov_b64_e32 v[16:17], v[0:1]
	v_mov_b64_e32 v[60:61], v[12:13]
	v_mov_b64_e32 v[58:59], v[10:11]
	v_mov_b64_e32 v[56:57], v[8:9]
	v_mov_b64_e32 v[54:55], v[6:7]
	v_mov_b64_e32 v[52:53], v[4:5]
	v_mov_b64_e32 v[50:51], v[2:3]
	v_mov_b64_e32 v[48:49], v[0:1]
	v_mov_b64_e32 v[92:93], v[12:13]
	v_mov_b64_e32 v[90:91], v[10:11]
	v_mov_b64_e32 v[88:89], v[8:9]
	v_mov_b64_e32 v[86:87], v[6:7]
	v_mov_b64_e32 v[84:85], v[4:5]
	v_mov_b64_e32 v[82:83], v[2:3]
	v_mov_b64_e32 v[80:81], v[0:1]
	v_mov_b64_e32 v[124:125], v[12:13]
	v_mov_b64_e32 v[122:123], v[10:11]
	v_mov_b64_e32 v[120:121], v[8:9]
	v_mov_b64_e32 v[118:119], v[6:7]
	v_mov_b64_e32 v[116:117], v[4:5]
	v_mov_b64_e32 v[114:115], v[2:3]
	v_mov_b64_e32 v[112:113], v[0:1]
	v_mov_b64_e32 v[44:45], v[12:13]
	v_mov_b64_e32 v[42:43], v[10:11]
	v_mov_b64_e32 v[40:41], v[8:9]
	v_mov_b64_e32 v[38:39], v[6:7]
	v_mov_b64_e32 v[36:37], v[4:5]
	v_mov_b64_e32 v[34:35], v[2:3]
	v_mov_b64_e32 v[32:33], v[0:1]
	v_mov_b64_e32 v[76:77], v[12:13]
	v_mov_b64_e32 v[74:75], v[10:11]
	v_mov_b64_e32 v[72:73], v[8:9]
	v_mov_b64_e32 v[70:71], v[6:7]
	v_mov_b64_e32 v[68:69], v[4:5]
	v_mov_b64_e32 v[66:67], v[2:3]
	v_mov_b64_e32 v[64:65], v[0:1]
	v_mov_b64_e32 v[108:109], v[12:13]
	v_mov_b64_e32 v[106:107], v[10:11]
	v_mov_b64_e32 v[104:105], v[8:9]
	v_mov_b64_e32 v[102:103], v[6:7]
	v_mov_b64_e32 v[100:101], v[4:5]
	v_mov_b64_e32 v[98:99], v[2:3]
	v_mov_b64_e32 v[96:97], v[0:1]
	v_mov_b64_e32 v[140:141], v[12:13]
	v_mov_b64_e32 v[138:139], v[10:11]
	v_mov_b64_e32 v[136:137], v[8:9]
	v_mov_b64_e32 v[134:135], v[6:7]
	v_mov_b64_e32 v[132:133], v[4:5]
	v_mov_b64_e32 v[130:131], v[2:3]
	v_mov_b64_e32 v[128:129], v[0:1]
	v_mov_b32_e32 v209, 0xf149f2ca
	v_mov_b32_e32 v207, 0
	s_mov_b32 s25, 0
	s_waitcnt lgkmcnt(0)
	s_barrier
	v_and_b32_e32 v2, 31, v204
	v_bfe_u32 v15, v204, 5, 1
	v_lshlrev_b32_e32 v15, 4, v15
	v_or_b32_e32 v13, s12, v2
	v_mul_u32_u24_e32 v1, 0x90, v2
	v_mad_u32_u24 v0, v2, s30, v15
	v_mul_lo_u32 v13, v13, s30
	v_add_u32_e32 v0, v0, v205
	v_add3_u32 v1, v1, v15, v205
	v_add3_u32 v13, v206, v13, v15
	v_bfe_u32 v15, v204, 2, 2
	v_and_b32_e32 v2, 12, v204
	v_cmp_ne_u32_e32 vcc, 2, v15
	s_movk_i32 s24, 0x480
	v_ashrrev_i32_e32 v211, 6, v204
	v_cndmask_b32_e32 v2, 4, v2, vcc
	v_cmp_ne_u32_e32 vcc, 1, v15
	v_mul_lo_u32 v211, v211, s24
	s_nop 0
	v_cndmask_b32_e32 v15, 8, v2, vcc
	v_and_or_b32 v2, v204, 51, v15
	v_lshlrev_b32_e32 v2, 1, v2
	v_add3_u32 v2, v205, v211, v2
	v_and_b32_e32 v206, 63, v204
	v_ashrrev_i32_e32 v252, 6, v204
	s_movk_i32 s24, 0x1400
	v_lshlrev_b32_e32 v252, 4, v252
	v_mad_u32_u24 v252, v206, s24, v252
	v_lshlrev_b32_e32 v206, 2, v206
	v_add_u32_e32 v206, 0x400, v206
	v_mov_b32_e32 v12, v0
	ds_read_b128 v[228:231], v12 offset:0
	ds_read_b128 v[232:235], v12 offset:32
	ds_read_b128 v[236:239], v12 offset:64
	ds_read_b128 v[240:243], v12 offset:96
	ds_read_b128 v[244:247], v13 offset:0
	ds_read_b128 v[248:251], v13 offset:32
	ds_read_b128 v[4:7], v13 offset:64
	ds_read_b128 v[8:11], v13 offset:96
.LBB0_747:
	s_add_i32 s23, s25, 1
	s_and_b32 s27, s25, 1
	s_mul_i32 s26, s27, 0x4400
	s_mul_i32 s31, s27, 0x4800
	v_add_u32_e32 v12, s26, v0
	v_add_u32_e32 v14, s31, v1
	ds_read_b128 v[184:187], v14 offset:34816
	ds_read_b128 v[188:191], v14 offset:39424
	ds_read_b128 v[192:195], v14 offset:44032
	ds_read_b128 v[196:199], v14 offset:48640
	ds_read_b128 v[200:203], v14 offset:34848
	ds_read_b128 v[212:215], v14 offset:39456
	ds_read_b128 v[216:219], v14 offset:44064
	s_cmp_gt_u32 s25, 2
	s_waitcnt lgkmcnt(7)
	ds_read_b128 v[220:223], v14 offset:48672
	s_cbranch_scc1 .Lat2_noload
	v_mfma_f32_32x32x16_bf16 v[144:159], v[228:231], v[244:247], 0
	s_mov_b32 s26, s15
	s_mov_b32 s31, s9
	s_add_i32 s26, s26, s22
	s_add_i32 s31, s31, s10
	s_mul_hi_i32 s37, s26, 0x1400
	s_mul_i32 s36, s26, 0x1400
	s_add_i32 s31, s31, s22
	s_add_u32 s36, s0, s36
	s_addc_u32 s37, s1, s37
	s_add_i32 s31, s31, 64
	global_load_dwordx4 v[176:179], v252, s[36:37] offset:2048
	global_load_dwordx4 v[180:183], v252, s[36:37] offset:2176
	s_mul_hi_i32 s37, s31, 0x1400
	s_mul_i32 s36, s31, 0x1400
	s_add_u32 s36, s0, s36
	v_mfma_f32_32x32x16_bf16 v[144:159], v[232:235], v[248:251], v[144:159]
	s_addc_u32 s37, s1, s37
	v_readfirstlane_b32 s2, v205
	s_xor_b32 s3, s27, 1
	s_mul_i32 s3, s3, 0x4400
	s_add_i32 s2, s2, s13
	s_add_i32 s2, s2, s3
	s_add_i32 m0, s2, 0
	s_nop 0
	global_load_lds_dword v206, s[36:37]
	s_add_u32 s36, s36, 0x1400
	s_addc_u32 s37, s37, 0
	s_add_i32 m0, s2, 272
	s_nop 0
	global_load_lds_dword v206, s[36:37]
	s_add_u32 s36, s36, 0x1400
	v_mfma_f32_32x32x16_bf16 v[144:159], v[236:239], v[4:7], v[144:159]
	s_addc_u32 s37, s37, 0
	s_add_i32 m0, s2, 544
	s_nop 0
	global_load_lds_dword v206, s[36:37]
	s_add_u32 s36, s36, 0x1400
	s_addc_u32 s37, s37, 0
	s_add_i32 m0, s2, 816
	s_nop 0
	global_load_lds_dword v206, s[36:37]
	s_add_u32 s36, s36, 0x1400
	s_addc_u32 s37, s37, 0
	s_add_i32 m0, s2, 1088
	s_nop 0
	global_load_lds_dword v206, s[36:37]
	s_add_u32 s36, s36, 0x1400
	v_mfma_f32_32x32x16_bf16 v[144:159], v[240:243], v[8:11], v[144:159]
	s_addc_u32 s37, s37, 0
	s_add_i32 m0, s2, 1360
	s_nop 0
	global_load_lds_dword v206, s[36:37]
	s_add_u32 s36, s36, 0x1400
	s_addc_u32 s37, s37, 0
	s_add_i32 m0, s2, 1632
	s_nop 0
	global_load_lds_dword v206, s[36:37]
	s_add_u32 s36, s36, 0x1400
	s_addc_u32 s37, s37, 0
	s_add_i32 m0, s2, 1904
	s_nop 0
	global_load_lds_dword v206, s[36:37]
	s_branch .Lat2_join

.Lat2_back1_s1:
	v_sub_f32_e32 v160, v160, v208
	v_sub_f32_e32 v161, v161, v208
	v_sub_f32_e32 v162, v162, v208
	v_sub_f32_e32 v163, v163, v208
	v_mfma_f32_32x32x16_bf16 v[96:111], v[188:191], v[144:147], v[96:111]
	v_exp_f32_e32 v160, v160
	v_exp_f32_e32 v161, v161
	v_exp_f32_e32 v162, v162
	v_exp_f32_e32 v163, v163
	v_sub_f32_e32 v164, v164, v208
	v_sub_f32_e32 v165, v165, v208
	v_sub_f32_e32 v166, v166, v208
	v_sub_f32_e32 v167, v167, v208
	v_mfma_f32_32x32x16_bf16 v[64:79], v[192:195], v[144:147], v[64:79]
	v_exp_f32_e32 v164, v164
	v_exp_f32_e32 v165, v165
	v_exp_f32_e32 v166, v166
	v_exp_f32_e32 v167, v167
	v_sub_f32_e32 v168, v168, v208
	v_sub_f32_e32 v169, v169, v208
	v_sub_f32_e32 v170, v170, v208
	v_sub_f32_e32 v171, v171, v208
	v_mfma_f32_32x32x16_bf16 v[32:47], v[196:199], v[144:147], v[32:47]
	v_exp_f32_e32 v168, v168
	v_exp_f32_e32 v169, v169
	v_exp_f32_e32 v170, v170
	v_exp_f32_e32 v171, v171
	v_sub_f32_e32 v172, v172, v208
	v_sub_f32_e32 v173, v173, v208
	v_sub_f32_e32 v174, v174, v208
	v_sub_f32_e32 v175, v175, v208
	v_mfma_f32_32x32x16_bf16 v[128:143], v[200:203], v[148:151], v[128:143]
	v_exp_f32_e32 v172, v172
	v_exp_f32_e32 v173, v173
	v_exp_f32_e32 v174, v174
	v_exp_f32_e32 v175, v175
	v_add_f32_e32 v15, v160, v161
	v_add_f32_e32 v211, v162, v163
	v_add_f32_e32 v15, v15, v211
	v_add_f32_e32 v211, v164, v165
	v_mfma_f32_32x32x16_bf16 v[96:111], v[212:215], v[148:151], v[96:111]
	v_add_f32_e32 v224, v166, v167
	v_add_f32_e32 v211, v211, v224
	v_add_f32_e32 v224, v168, v169
	v_add_f32_e32 v225, v170, v171
	v_add_f32_e32 v224, v224, v225
	v_add_f32_e32 v225, v172, v173
	v_add_f32_e32 v227, v174, v175
	v_add_f32_e32 v225, v225, v227
	v_add_f32_e32 v15, v15, v211
	v_add_f32_e32 v224, v224, v225
	v_add_f32_e32 v15, v15, v224
	v_add_f32_e32 v207, v207, v15
	v_cvt_pk_bf16_f32 v160, v160, v161
	v_cvt_pk_bf16_f32 v161, v162, v163
	v_cvt_pk_bf16_f32 v162, v164, v165
	v_cvt_pk_bf16_f32 v163, v166, v167
	v_cvt_pk_bf16_f32 v164, v168, v169
	v_cvt_pk_bf16_f32 v165, v170, v171
	v_cvt_pk_bf16_f32 v166, v172, v173
	v_cvt_pk_bf16_f32 v167, v174, v175
	v_mfma_f32_32x32x16_bf16 v[64:79], v[216:219], v[148:151], v[64:79]
	s_xor_b32 s24, s27, 1
	s_mulk_i32 s24, 0x4800
	s_waitcnt vmcnt(0)
	v_add_u32_e32 v15, s24, v2
	ds_write_b16 v15, v176 offset:34816
	ds_write_b16_d16_hi v15, v176 offset:34960
	ds_write_b16 v15, v177 offset:35104
	ds_write_b16_d16_hi v15, v177 offset:35248
	ds_write_b16 v15, v178 offset:35392
	ds_write_b16_d16_hi v15, v178 offset:35536
	ds_write_b16 v15, v179 offset:35680
	ds_write_b16_d16_hi v15, v179 offset:35824
	ds_write_b16 v15, v180 offset:44032
	ds_write_b16_d16_hi v15, v180 offset:44176
	ds_write_b16 v15, v181 offset:44320
	ds_write_b16_d16_hi v15, v181 offset:44464
	ds_write_b16 v15, v182 offset:44608
	ds_write_b16_d16_hi v15, v182 offset:44752
	ds_write_b16 v15, v183 offset:44896
	ds_write_b16_d16_hi v15, v183 offset:45040
	v_mfma_f32_32x32x16_bf16 v[32:47], v[220:223], v[148:151], v[32:47]
	s_add_i32 s22, s22, 64
	s_cmpk_lg_i32 s22, 0x100
	s_waitcnt vmcnt(0) lgkmcnt(0)
	s_barrier
	s_cbranch_scc0 .Lat2_last
	s_and_b32 s24, s23, 1
	s_mul_i32 s24, s24, 0x4400
	v_add_u32_e32 v12, s24, v0
	v_mfma_f32_32x32x16_bf16 v[112:127], v[184:187], v[160:163], v[112:127]
	ds_read_b128 v[228:231], v12 offset:0
	v_mfma_f32_32x32x16_bf16 v[80:95], v[188:191], v[160:163], v[80:95]
	ds_read_b128 v[232:235], v12 offset:32
	v_mfma_f32_32x32x16_bf16 v[48:63], v[192:195], v[160:163], v[48:63]
	ds_read_b128 v[236:239], v12 offset:64
	v_mfma_f32_32x32x16_bf16 v[16:31], v[196:199], v[160:163], v[16:31]
	ds_read_b128 v[240:243], v12 offset:96
	v_mfma_f32_32x32x16_bf16 v[112:127], v[200:203], v[164:167], v[112:127]
	ds_read_b128 v[244:247], v13 offset:0
	v_mfma_f32_32x32x16_bf16 v[80:95], v[212:215], v[164:167], v[80:95]
	ds_read_b128 v[248:251], v13 offset:32
	v_mfma_f32_32x32x16_bf16 v[48:63], v[216:219], v[164:167], v[48:63]
	ds_read_b128 v[4:7], v13 offset:64
	v_mfma_f32_32x32x16_bf16 v[16:31], v[220:223], v[164:167], v[16:31]
	ds_read_b128 v[8:11], v13 offset:96
	s_mov_b32 s25, s23
	s_branch .LBB0_747
